# BR branch epilogue rewritten as software pipeline: up to five row groups of G and Mg loads in flight, counted vmcnt
# baseline (speedup 1.0000x reference)
; #define PG8_BAR __builtin_amdgcn_s_barrier()
; #define PG8_BAR __builtin_amdgcn_s_barrier()
; template <class Epi, class Sched, bool ALIGN_EPI = true, class Hook = NoHook>
; __device__ __forceinline__ void gemm_phase_het(PG8_LAS unsigned char* lds, const GemmHet g, const Sched& S, const Epi& E, const Hook& H = Hook()) {
;     ...
;         if (!has_next) break;
; #pragma unroll
;         for (int a = 0; a < 2; ++a)
; #pragma unroll
;             for (int b = 0; b < 2; ++b)
; #pragma unroll
;                 for (int m = 0; m < 4; ++m)
; #pragma unroll
;                     for (int n = 0; n < 2; ++n) acc[a][b][m][n] = (f32x4){0.f, 0.f, 0.f, 0.f};
;         cur = nxt; cA = nA; cB = nB; hA = nhA; hB = nhB; nt = nnt; voffA[0] = nvA[0]; voffA[1] = nvA[1]; voffB[0] = nvB[0]; voffB[1] = nvB[1]; ++ui;
;         if constexpr (ALIGN_EPI) { if (wr == 1) PG8_BAR; }
.Lbrepi_done:
	s_and_b64 vcc, exec, s[38:39]
	s_mov_b32 s72, s70
	v_mov_b32_e32 v130, v172
	v_mov_b32_e32 v132, v170
	s_mov_b32 s73, s2
	s_mov_b32 s75, s45
	s_mov_b32 s74, s71
	s_mov_b64 s[52:53], s[14:15]
	s_mov_b64 s[54:55], s[46:47]
	s_mov_b64 s[40:41], s[42:43]
	s_mov_b64 s[50:51], s[20:21]
	v_mov_b32_e32 v140, v195
	v_mov_b32_e32 v141, v194
	s_cbranch_vccnz .LBB0_392

; __device__ __forceinline__ unsigned cvt_pk_f16(float lo, float hi) { f32x2 v = {lo, hi}; h16x2 b = __builtin_convertvector(v, h16x2); return __builtin_bit_cast(unsigned, b); }
;     __device__ __forceinline__ void operator()(const f32x4 (&acc)[2][2][4][2], const Unit& u, int wr, int wc, int fr, int fq) const {
;     ...
;         } else {
; #pragma unroll
;             for (int ai = 0; ai < 2; ++ai)
; #pragma unroll
;                 for (int mp = 0; mp < 2; ++mp) {
;                     h16x8 gv[2][2], pv[2][2];
; #pragma unroll
;                     for (int mm = 0; mm < 2; ++mm)
; #pragma unroll
;                         for (int bj = 0; bj < 2; ++bj) { const size_t row = (size_t)(row0 + ai * HALF + (2 * mp + mm) * 16);
;                             gv[mm][bj] = *(const h16x8*)(Gn + row * ldg + bj * HALF);
;                             if (n > 0) pv[mm][bj] = *(const h16x8*)(Mg + row * 1024 + col0 + bj * HALF); }
; #pragma unroll
;                     for (int mm = 0; mm < 2; ++mm)
; #pragma unroll
;                         for (int bj = 0; bj < 2; ++bj) { const int m = 2 * mp + mm; const size_t row = (size_t)(row0 + ai * HALF + m * 16);
;                             float o[8];
; #pragma unroll
;                             for (int e = 0; e < 8; ++e) { const float a = e < 4 ? acc[ai][bj][m][0][e] : acc[ai][bj][m][1][e - 4]; o[e] = a * (float)gv[mm][bj][e]; }
;                             if (n > 0) {
; #pragma unroll
;                                 for (int e = 0; e < 8; ++e) o[e] += (float)pv[mm][bj][e]; }
;                             u32x4 w; w.x = cvt_pk_f16(o[0], o[1]); w.y = cvt_pk_f16(o[2], o[3]); w.z = cvt_pk_f16(o[4], o[5]); w.w = cvt_pk_f16(o[6], o[7]);
;                             *(u32x4*)(Mg + row * 1024 + col0 + bj * HALF) = w; }
.LBB0_324:
	v_lshl_or_b32 v178, s73, 8, v165
	v_readlane_b32 s0, v253, 62
	v_ashrrev_i32_e32 v179, 31, v178
	v_readlane_b32 s1, v253, 63
	v_lshl_add_u32 v176, s75, 8, v192
	s_cmp_lt_u32 s72, 4
	v_lshl_add_u64 v[174:175], v[178:179], 1, s[0:1]
	s_mov_b64 s[0:1], -1
	s_cbranch_scc1 .LBB0_390
	s_and_b32 s0, s72, 3
	s_cmp_eq_u32 s0, 0
	s_cbranch_scc1 .Lbrepi_n0
	v_readlane_b32 s40, v254, 46
	v_readlane_b32 s41, v254, 47
	v_mov_b32_e32 v241, 0
	s_nop 1
	v_lshl_add_u64 v[180:181], v[178:179], 1, s[40:41]
	v_mov_b32_e32 v238, v176
	v_mad_i64_i32 v[234:235], s[0:1], v238, s91, v[174:175]
	v_lshlrev_b32_e32 v240, 11, v238
	v_lshl_add_u64 v[236:237], v[180:181], 0, v[240:241]
	global_load_dwordx4 v[130:133], v[234:235], off
	global_load_dwordx4 v[138:141], v[236:237], off
	global_load_dwordx4 v[134:137], v[234:235], off offset:256
	global_load_dwordx4 v[142:145], v[236:237], off offset:256
	v_add_u32_e32 v238, 16, v176
	v_mad_i64_i32 v[234:235], s[0:1], v238, s91, v[174:175]
	v_lshlrev_b32_e32 v240, 11, v238
	v_lshl_add_u64 v[236:237], v[180:181], 0, v[240:241]
	global_load_dwordx4 v[146:149], v[234:235], off
	global_load_dwordx4 v[154:157], v[236:237], off
	global_load_dwordx4 v[150:153], v[234:235], off offset:256
	global_load_dwordx4 v[158:161], v[236:237], off offset:256
	s_waitcnt vmcnt(4)
	v_mov_b32_e32 v238, v176
	v_lshlrev_b32_e32 v240, 11, v238
	v_lshl_add_u64 v[236:237], v[180:181], 0, v[240:241]
	v_cvt_f32_f16_e32 v182, v130
	v_cvt_f32_f16_sdwa v183, v130 dst_sel:DWORD dst_unused:UNUSED_PAD src0_sel:WORD_1
	v_cvt_f32_f16_e32 v184, v131
	v_cvt_f32_f16_sdwa v185, v131 dst_sel:DWORD dst_unused:UNUSED_PAD src0_sel:WORD_1
	v_cvt_f32_f16_e32 v186, v132
	v_cvt_f32_f16_sdwa v187, v132 dst_sel:DWORD dst_unused:UNUSED_PAD src0_sel:WORD_1
	v_cvt_f32_f16_e32 v188, v133
	v_cvt_f32_f16_sdwa v189, v133 dst_sel:DWORD dst_unused:UNUSED_PAD src0_sel:WORD_1
	v_cvt_f32_f16_e32 v196, v138
	v_cvt_f32_f16_sdwa v197, v138 dst_sel:DWORD dst_unused:UNUSED_PAD src0_sel:WORD_1
	v_cvt_f32_f16_e32 v198, v139
	v_cvt_f32_f16_sdwa v199, v139 dst_sel:DWORD dst_unused:UNUSED_PAD src0_sel:WORD_1
	v_cvt_f32_f16_e32 v200, v140
	v_cvt_f32_f16_sdwa v201, v140 dst_sel:DWORD dst_unused:UNUSED_PAD src0_sel:WORD_1
	v_cvt_f32_f16_e32 v202, v141
	v_cvt_f32_f16_sdwa v203, v141 dst_sel:DWORD dst_unused:UNUSED_PAD src0_sel:WORD_1
	v_pk_mul_f32 v[182:183], v[126:127], v[182:183]
	v_pk_mul_f32 v[184:185], v[128:129], v[184:185]
	v_pk_mul_f32 v[186:187], v[122:123], v[186:187]
	v_pk_mul_f32 v[188:189], v[124:125], v[188:189]
	v_pk_add_f32 v[182:183], v[182:183], v[196:197]
	v_pk_add_f32 v[184:185], v[184:185], v[198:199]
	v_pk_add_f32 v[186:187], v[186:187], v[200:201]
	v_pk_add_f32 v[188:189], v[188:189], v[202:203]
	v_cvt_pk_f16_f32 v126, v182, v183
	v_cvt_pk_f16_f32 v127, v184, v185
	v_cvt_pk_f16_f32 v128, v186, v187
	v_cvt_pk_f16_f32 v129, v188, v189
	global_store_dwordx4 v[236:237], v[126:129], off
	v_cvt_f32_f16_e32 v182, v134
	v_cvt_f32_f16_sdwa v183, v134 dst_sel:DWORD dst_unused:UNUSED_PAD src0_sel:WORD_1
	v_cvt_f32_f16_e32 v184, v135
	v_cvt_f32_f16_sdwa v185, v135 dst_sel:DWORD dst_unused:UNUSED_PAD src0_sel:WORD_1
	v_cvt_f32_f16_e32 v186, v136
	v_cvt_f32_f16_sdwa v187, v136 dst_sel:DWORD dst_unused:UNUSED_PAD src0_sel:WORD_1
	v_cvt_f32_f16_e32 v188, v137
	v_cvt_f32_f16_sdwa v189, v137 dst_sel:DWORD dst_unused:UNUSED_PAD src0_sel:WORD_1
	v_cvt_f32_f16_e32 v196, v142
	v_cvt_f32_f16_sdwa v197, v142 dst_sel:DWORD dst_unused:UNUSED_PAD src0_sel:WORD_1
	v_cvt_f32_f16_e32 v198, v143
	v_cvt_f32_f16_sdwa v199, v143 dst_sel:DWORD dst_unused:UNUSED_PAD src0_sel:WORD_1
	v_cvt_f32_f16_e32 v200, v144
	v_cvt_f32_f16_sdwa v201, v144 dst_sel:DWORD dst_unused:UNUSED_PAD src0_sel:WORD_1
	v_cvt_f32_f16_e32 v202, v145
	v_cvt_f32_f16_sdwa v203, v145 dst_sel:DWORD dst_unused:UNUSED_PAD src0_sel:WORD_1
	v_pk_mul_f32 v[182:183], v[118:119], v[182:183]
	v_pk_mul_f32 v[184:185], v[120:121], v[184:185]
	v_pk_mul_f32 v[186:187], v[114:115], v[186:187]
	v_pk_mul_f32 v[188:189], v[116:117], v[188:189]
	v_pk_add_f32 v[182:183], v[182:183], v[196:197]
	v_pk_add_f32 v[184:185], v[184:185], v[198:199]
	v_pk_add_f32 v[186:187], v[186:187], v[200:201]
	v_pk_add_f32 v[188:189], v[188:189], v[202:203]
	v_cvt_pk_f16_f32 v118, v182, v183
	v_cvt_pk_f16_f32 v119, v184, v185
	v_cvt_pk_f16_f32 v120, v186, v187
	v_cvt_pk_f16_f32 v121, v188, v189
	global_store_dwordx4 v[236:237], v[118:121], off offset:256
	v_add_u32_e32 v238, 32, v176
	v_mad_i64_i32 v[234:235], s[0:1], v238, s91, v[174:175]
	v_lshlrev_b32_e32 v240, 11, v238
	v_lshl_add_u64 v[236:237], v[180:181], 0, v[240:241]
	global_load_dwordx4 v[130:133], v[234:235], off
	global_load_dwordx4 v[138:141], v[236:237], off
	global_load_dwordx4 v[134:137], v[234:235], off offset:256
	global_load_dwordx4 v[142:145], v[236:237], off offset:256
	s_nop 1
	v_add_u32_e32 v238, 48, v176
	v_mad_i64_i32 v[234:235], s[0:1], v238, s91, v[174:175]
	v_lshlrev_b32_e32 v240, 11, v238
	v_lshl_add_u64 v[236:237], v[180:181], 0, v[240:241]
	global_load_dwordx4 v[126:129], v[234:235], off
	global_load_dwordx4 v[118:121], v[236:237], off
	global_load_dwordx4 v[122:125], v[234:235], off offset:256
	global_load_dwordx4 v[114:117], v[236:237], off offset:256
	s_waitcnt vmcnt(10)
; __device__ __forceinline__ unsigned cvt_pk_f16(float lo, float hi) { f32x2 v = {lo, hi}; h16x2 b = __builtin_convertvector(v, h16x2); return __builtin_bit_cast(unsigned, b); }
;     __device__ __forceinline__ void operator()(const f32x4 (&acc)[2][2][4][2], const Unit& u, int wr, int wc, int fr, int fq) const {
;     ...
; #pragma unroll
;             for (int ai = 0; ai < 2; ++ai)
; #pragma unroll
;                 for (int mp = 0; mp < 2; ++mp) {
;                     h16x8 gv[2][2], pv[2][2];
; #pragma unroll
;                     for (int mm = 0; mm < 2; ++mm)
; #pragma unroll
;                         for (int bj = 0; bj < 2; ++bj) { const size_t row = (size_t)(row0 + ai * HALF + (2 * mp + mm) * 16);
;                             gv[mm][bj] = *(const h16x8*)(Gn + row * ldg + bj * HALF);
;                             if (n > 0) pv[mm][bj] = *(const h16x8*)(Mg + row * 1024 + col0 + bj * HALF); }
; #pragma unroll
;                     for (int mm = 0; mm < 2; ++mm)
; #pragma unroll
;                         for (int bj = 0; bj < 2; ++bj) { const int m = 2 * mp + mm; const size_t row = (size_t)(row0 + ai * HALF + m * 16);
;                             float o[8];
; #pragma unroll
;                             for (int e = 0; e < 8; ++e) { const float a = e < 4 ? acc[ai][bj][m][0][e] : acc[ai][bj][m][1][e - 4]; o[e] = a * (float)gv[mm][bj][e]; }
;                             if (n > 0) {
; #pragma unroll
;                                 for (int e = 0; e < 8; ++e) o[e] += (float)pv[mm][bj][e]; }
;                             u32x4 w; w.x = cvt_pk_f16(o[0], o[1]); w.y = cvt_pk_f16(o[2], o[3]); w.z = cvt_pk_f16(o[4], o[5]); w.w = cvt_pk_f16(o[6], o[7]);
;                             *(u32x4*)(Mg + row * 1024 + col0 + bj * HALF) = w; }
	v_add_u32_e32 v238, 16, v176
	v_lshlrev_b32_e32 v240, 11, v238
	v_lshl_add_u64 v[236:237], v[180:181], 0, v[240:241]
	v_cvt_f32_f16_e32 v182, v146
	v_cvt_f32_f16_sdwa v183, v146 dst_sel:DWORD dst_unused:UNUSED_PAD src0_sel:WORD_1
	v_cvt_f32_f16_e32 v184, v147
	v_cvt_f32_f16_sdwa v185, v147 dst_sel:DWORD dst_unused:UNUSED_PAD src0_sel:WORD_1
	v_cvt_f32_f16_e32 v186, v148
	v_cvt_f32_f16_sdwa v187, v148 dst_sel:DWORD dst_unused:UNUSED_PAD src0_sel:WORD_1
	v_cvt_f32_f16_e32 v188, v149
	v_cvt_f32_f16_sdwa v189, v149 dst_sel:DWORD dst_unused:UNUSED_PAD src0_sel:WORD_1
	v_cvt_f32_f16_e32 v196, v154
	v_cvt_f32_f16_sdwa v197, v154 dst_sel:DWORD dst_unused:UNUSED_PAD src0_sel:WORD_1
	v_cvt_f32_f16_e32 v198, v155
	v_cvt_f32_f16_sdwa v199, v155 dst_sel:DWORD dst_unused:UNUSED_PAD src0_sel:WORD_1
	v_cvt_f32_f16_e32 v200, v156
	v_cvt_f32_f16_sdwa v201, v156 dst_sel:DWORD dst_unused:UNUSED_PAD src0_sel:WORD_1
	v_cvt_f32_f16_e32 v202, v157
	v_cvt_f32_f16_sdwa v203, v157 dst_sel:DWORD dst_unused:UNUSED_PAD src0_sel:WORD_1
	v_pk_mul_f32 v[182:183], v[110:111], v[182:183]
	v_pk_mul_f32 v[184:185], v[112:113], v[184:185]
	v_pk_mul_f32 v[186:187], v[106:107], v[186:187]
	v_pk_mul_f32 v[188:189], v[108:109], v[188:189]
	v_pk_add_f32 v[182:183], v[182:183], v[196:197]
	v_pk_add_f32 v[184:185], v[184:185], v[198:199]
	v_pk_add_f32 v[186:187], v[186:187], v[200:201]
	v_pk_add_f32 v[188:189], v[188:189], v[202:203]
	v_cvt_pk_f16_f32 v110, v182, v183
	v_cvt_pk_f16_f32 v111, v184, v185
	v_cvt_pk_f16_f32 v112, v186, v187
	v_cvt_pk_f16_f32 v113, v188, v189
	global_store_dwordx4 v[236:237], v[110:113], off
	v_cvt_f32_f16_e32 v182, v150
	v_cvt_f32_f16_sdwa v183, v150 dst_sel:DWORD dst_unused:UNUSED_PAD src0_sel:WORD_1
	v_cvt_f32_f16_e32 v184, v151
	v_cvt_f32_f16_sdwa v185, v151 dst_sel:DWORD dst_unused:UNUSED_PAD src0_sel:WORD_1
	v_cvt_f32_f16_e32 v186, v152
	v_cvt_f32_f16_sdwa v187, v152 dst_sel:DWORD dst_unused:UNUSED_PAD src0_sel:WORD_1
	v_cvt_f32_f16_e32 v188, v153
	v_cvt_f32_f16_sdwa v189, v153 dst_sel:DWORD dst_unused:UNUSED_PAD src0_sel:WORD_1
	v_cvt_f32_f16_e32 v196, v158
	v_cvt_f32_f16_sdwa v197, v158 dst_sel:DWORD dst_unused:UNUSED_PAD src0_sel:WORD_1
	v_cvt_f32_f16_e32 v198, v159
	v_cvt_f32_f16_sdwa v199, v159 dst_sel:DWORD dst_unused:UNUSED_PAD src0_sel:WORD_1
	v_cvt_f32_f16_e32 v200, v160
	v_cvt_f32_f16_sdwa v201, v160 dst_sel:DWORD dst_unused:UNUSED_PAD src0_sel:WORD_1
	v_cvt_f32_f16_e32 v202, v161
	v_cvt_f32_f16_sdwa v203, v161 dst_sel:DWORD dst_unused:UNUSED_PAD src0_sel:WORD_1
	v_pk_mul_f32 v[182:183], v[102:103], v[182:183]
	v_pk_mul_f32 v[184:185], v[104:105], v[184:185]
	v_pk_mul_f32 v[186:187], v[98:99], v[186:187]
	v_pk_mul_f32 v[188:189], v[100:101], v[188:189]
	v_pk_add_f32 v[182:183], v[182:183], v[196:197]
	v_pk_add_f32 v[184:185], v[184:185], v[198:199]
	v_pk_add_f32 v[186:187], v[186:187], v[200:201]
	v_pk_add_f32 v[188:189], v[188:189], v[202:203]
	v_cvt_pk_f16_f32 v102, v182, v183
	v_cvt_pk_f16_f32 v103, v184, v185
	v_cvt_pk_f16_f32 v104, v186, v187
	v_cvt_pk_f16_f32 v105, v188, v189
	global_store_dwordx4 v[236:237], v[102:105], off offset:256
	v_add_u32_e32 v238, 128, v176
	v_mad_i64_i32 v[234:235], s[0:1], v238, s91, v[174:175]
	v_lshlrev_b32_e32 v240, 11, v238
	v_lshl_add_u64 v[236:237], v[180:181], 0, v[240:241]
	global_load_dwordx4 v[146:149], v[234:235], off
	global_load_dwordx4 v[154:157], v[236:237], off
	global_load_dwordx4 v[150:153], v[234:235], off offset:256
	global_load_dwordx4 v[158:161], v[236:237], off offset:256
	s_nop 1
	v_add_u32_e32 v238, 144, v176
	v_mad_i64_i32 v[234:235], s[0:1], v238, s91, v[174:175]
	v_lshlrev_b32_e32 v240, 11, v238
	v_lshl_add_u64 v[236:237], v[180:181], 0, v[240:241]
	global_load_dwordx4 v[110:113], v[234:235], off
	global_load_dwordx4 v[102:105], v[236:237], off
	global_load_dwordx4 v[106:109], v[234:235], off offset:256
	global_load_dwordx4 v[98:101], v[236:237], off offset:256
	s_waitcnt vmcnt(14)
	v_add_u32_e32 v238, 32, v176
	v_lshlrev_b32_e32 v240, 11, v238
	v_lshl_add_u64 v[236:237], v[180:181], 0, v[240:241]
	v_cvt_f32_f16_e32 v182, v130
	v_cvt_f32_f16_sdwa v183, v130 dst_sel:DWORD dst_unused:UNUSED_PAD src0_sel:WORD_1
	v_cvt_f32_f16_e32 v184, v131
	v_cvt_f32_f16_sdwa v185, v131 dst_sel:DWORD dst_unused:UNUSED_PAD src0_sel:WORD_1
	v_cvt_f32_f16_e32 v186, v132
	v_cvt_f32_f16_sdwa v187, v132 dst_sel:DWORD dst_unused:UNUSED_PAD src0_sel:WORD_1
	v_cvt_f32_f16_e32 v188, v133
	v_cvt_f32_f16_sdwa v189, v133 dst_sel:DWORD dst_unused:UNUSED_PAD src0_sel:WORD_1
	v_cvt_f32_f16_e32 v196, v138
	v_cvt_f32_f16_sdwa v197, v138 dst_sel:DWORD dst_unused:UNUSED_PAD src0_sel:WORD_1
	v_cvt_f32_f16_e32 v198, v139
	v_cvt_f32_f16_sdwa v199, v139 dst_sel:DWORD dst_unused:UNUSED_PAD src0_sel:WORD_1
	v_cvt_f32_f16_e32 v200, v140
	v_cvt_f32_f16_sdwa v201, v140 dst_sel:DWORD dst_unused:UNUSED_PAD src0_sel:WORD_1
	v_cvt_f32_f16_e32 v202, v141
	v_cvt_f32_f16_sdwa v203, v141 dst_sel:DWORD dst_unused:UNUSED_PAD src0_sel:WORD_1
	v_pk_mul_f32 v[182:183], v[92:93], v[182:183]
	v_pk_mul_f32 v[184:185], v[94:95], v[184:185]
	v_pk_mul_f32 v[186:187], v[88:89], v[186:187]
	v_pk_mul_f32 v[188:189], v[90:91], v[188:189]
	v_pk_add_f32 v[182:183], v[182:183], v[196:197]
	v_pk_add_f32 v[184:185], v[184:185], v[198:199]
	v_pk_add_f32 v[186:187], v[186:187], v[200:201]
	v_pk_add_f32 v[188:189], v[188:189], v[202:203]
	v_cvt_pk_f16_f32 v92, v182, v183
	v_cvt_pk_f16_f32 v93, v184, v185
	v_cvt_pk_f16_f32 v94, v186, v187
	v_cvt_pk_f16_f32 v95, v188, v189
	global_store_dwordx4 v[236:237], v[92:95], off
	v_cvt_f32_f16_e32 v182, v134
	v_cvt_f32_f16_sdwa v183, v134 dst_sel:DWORD dst_unused:UNUSED_PAD src0_sel:WORD_1
	v_cvt_f32_f16_e32 v184, v135
; __device__ __forceinline__ unsigned cvt_pk_f16(float lo, float hi) { f32x2 v = {lo, hi}; h16x2 b = __builtin_convertvector(v, h16x2); return __builtin_bit_cast(unsigned, b); }
;     __device__ __forceinline__ void operator()(const f32x4 (&acc)[2][2][4][2], const Unit& u, int wr, int wc, int fr, int fq) const {
;     ...
; #pragma unroll
;             for (int ai = 0; ai < 2; ++ai)
; #pragma unroll
;                 for (int mp = 0; mp < 2; ++mp) {
;                     h16x8 gv[2][2], pv[2][2];
; #pragma unroll
;                     for (int mm = 0; mm < 2; ++mm)
; #pragma unroll
;                         for (int bj = 0; bj < 2; ++bj) { const size_t row = (size_t)(row0 + ai * HALF + (2 * mp + mm) * 16);
;                             gv[mm][bj] = *(const h16x8*)(Gn + row * ldg + bj * HALF);
;                             if (n > 0) pv[mm][bj] = *(const h16x8*)(Mg + row * 1024 + col0 + bj * HALF); }
; #pragma unroll
;                     for (int mm = 0; mm < 2; ++mm)
; #pragma unroll
;                         for (int bj = 0; bj < 2; ++bj) { const int m = 2 * mp + mm; const size_t row = (size_t)(row0 + ai * HALF + m * 16);
;                             float o[8];
; #pragma unroll
;                             for (int e = 0; e < 8; ++e) { const float a = e < 4 ? acc[ai][bj][m][0][e] : acc[ai][bj][m][1][e - 4]; o[e] = a * (float)gv[mm][bj][e]; }
;                             if (n > 0) {
; #pragma unroll
;                                 for (int e = 0; e < 8; ++e) o[e] += (float)pv[mm][bj][e]; }
;                             u32x4 w; w.x = cvt_pk_f16(o[0], o[1]); w.y = cvt_pk_f16(o[2], o[3]); w.z = cvt_pk_f16(o[4], o[5]); w.w = cvt_pk_f16(o[6], o[7]);
;                             *(u32x4*)(Mg + row * 1024 + col0 + bj * HALF) = w; }
	v_cvt_f32_f16_sdwa v185, v135 dst_sel:DWORD dst_unused:UNUSED_PAD src0_sel:WORD_1
	v_cvt_f32_f16_e32 v186, v136
	v_cvt_f32_f16_sdwa v187, v136 dst_sel:DWORD dst_unused:UNUSED_PAD src0_sel:WORD_1
	v_cvt_f32_f16_e32 v188, v137
	v_cvt_f32_f16_sdwa v189, v137 dst_sel:DWORD dst_unused:UNUSED_PAD src0_sel:WORD_1
	v_cvt_f32_f16_e32 v196, v142
	v_cvt_f32_f16_sdwa v197, v142 dst_sel:DWORD dst_unused:UNUSED_PAD src0_sel:WORD_1
	v_cvt_f32_f16_e32 v198, v143
	v_cvt_f32_f16_sdwa v199, v143 dst_sel:DWORD dst_unused:UNUSED_PAD src0_sel:WORD_1
	v_cvt_f32_f16_e32 v200, v144
	v_cvt_f32_f16_sdwa v201, v144 dst_sel:DWORD dst_unused:UNUSED_PAD src0_sel:WORD_1
	v_cvt_f32_f16_e32 v202, v145
	v_cvt_f32_f16_sdwa v203, v145 dst_sel:DWORD dst_unused:UNUSED_PAD src0_sel:WORD_1
	v_pk_mul_f32 v[182:183], v[84:85], v[182:183]
	v_pk_mul_f32 v[184:185], v[86:87], v[184:185]
	v_pk_mul_f32 v[186:187], v[80:81], v[186:187]
	v_pk_mul_f32 v[188:189], v[82:83], v[188:189]
	v_pk_add_f32 v[182:183], v[182:183], v[196:197]
	v_pk_add_f32 v[184:185], v[184:185], v[198:199]
	v_pk_add_f32 v[186:187], v[186:187], v[200:201]
	v_pk_add_f32 v[188:189], v[188:189], v[202:203]
	v_cvt_pk_f16_f32 v84, v182, v183
	v_cvt_pk_f16_f32 v85, v184, v185
	v_cvt_pk_f16_f32 v86, v186, v187
	v_cvt_pk_f16_f32 v87, v188, v189
	global_store_dwordx4 v[236:237], v[84:87], off offset:256
	v_add_u32_e32 v238, 160, v176
	v_mad_i64_i32 v[234:235], s[0:1], v238, s91, v[174:175]
	v_lshlrev_b32_e32 v240, 11, v238
	v_lshl_add_u64 v[236:237], v[180:181], 0, v[240:241]
	global_load_dwordx4 v[130:133], v[234:235], off
	global_load_dwordx4 v[138:141], v[236:237], off
	global_load_dwordx4 v[134:137], v[234:235], off offset:256
	global_load_dwordx4 v[142:145], v[236:237], off offset:256
	s_nop 1
	v_add_u32_e32 v238, 176, v176
	v_mad_i64_i32 v[234:235], s[0:1], v238, s91, v[174:175]
	v_lshlrev_b32_e32 v240, 11, v238
	v_lshl_add_u64 v[236:237], v[180:181], 0, v[240:241]
	global_load_dwordx4 v[92:95], v[234:235], off
	global_load_dwordx4 v[84:87], v[236:237], off
	global_load_dwordx4 v[88:91], v[234:235], off offset:256
	global_load_dwordx4 v[80:83], v[236:237], off offset:256
	s_waitcnt vmcnt(20)
	v_add_u32_e32 v238, 48, v176
	v_lshlrev_b32_e32 v240, 11, v238
	v_lshl_add_u64 v[236:237], v[180:181], 0, v[240:241]
	v_cvt_f32_f16_e32 v182, v126
	v_cvt_f32_f16_sdwa v183, v126 dst_sel:DWORD dst_unused:UNUSED_PAD src0_sel:WORD_1
	v_cvt_f32_f16_e32 v184, v127
	v_cvt_f32_f16_sdwa v185, v127 dst_sel:DWORD dst_unused:UNUSED_PAD src0_sel:WORD_1
	v_cvt_f32_f16_e32 v186, v128
	v_cvt_f32_f16_sdwa v187, v128 dst_sel:DWORD dst_unused:UNUSED_PAD src0_sel:WORD_1
	v_cvt_f32_f16_e32 v188, v129
	v_cvt_f32_f16_sdwa v189, v129 dst_sel:DWORD dst_unused:UNUSED_PAD src0_sel:WORD_1
	v_cvt_f32_f16_e32 v196, v118
	v_cvt_f32_f16_sdwa v197, v118 dst_sel:DWORD dst_unused:UNUSED_PAD src0_sel:WORD_1
	v_cvt_f32_f16_e32 v198, v119
	v_cvt_f32_f16_sdwa v199, v119 dst_sel:DWORD dst_unused:UNUSED_PAD src0_sel:WORD_1
	v_cvt_f32_f16_e32 v200, v120
	v_cvt_f32_f16_sdwa v201, v120 dst_sel:DWORD dst_unused:UNUSED_PAD src0_sel:WORD_1
	v_cvt_f32_f16_e32 v202, v121
	v_cvt_f32_f16_sdwa v203, v121 dst_sel:DWORD dst_unused:UNUSED_PAD src0_sel:WORD_1
	v_pk_mul_f32 v[182:183], v[76:77], v[182:183]
	v_pk_mul_f32 v[184:185], v[78:79], v[184:185]
	v_pk_mul_f32 v[186:187], v[72:73], v[186:187]
	v_pk_mul_f32 v[188:189], v[74:75], v[188:189]
	v_pk_add_f32 v[182:183], v[182:183], v[196:197]
	v_pk_add_f32 v[184:185], v[184:185], v[198:199]
	v_pk_add_f32 v[186:187], v[186:187], v[200:201]
	v_pk_add_f32 v[188:189], v[188:189], v[202:203]
	v_cvt_pk_f16_f32 v76, v182, v183
	v_cvt_pk_f16_f32 v77, v184, v185
	v_cvt_pk_f16_f32 v78, v186, v187
	v_cvt_pk_f16_f32 v79, v188, v189
	global_store_dwordx4 v[236:237], v[76:79], off
	v_cvt_f32_f16_e32 v182, v122
	v_cvt_f32_f16_sdwa v183, v122 dst_sel:DWORD dst_unused:UNUSED_PAD src0_sel:WORD_1
	v_cvt_f32_f16_e32 v184, v123
	v_cvt_f32_f16_sdwa v185, v123 dst_sel:DWORD dst_unused:UNUSED_PAD src0_sel:WORD_1
	v_cvt_f32_f16_e32 v186, v124
	v_cvt_f32_f16_sdwa v187, v124 dst_sel:DWORD dst_unused:UNUSED_PAD src0_sel:WORD_1
	v_cvt_f32_f16_e32 v188, v125
	v_cvt_f32_f16_sdwa v189, v125 dst_sel:DWORD dst_unused:UNUSED_PAD src0_sel:WORD_1
	v_cvt_f32_f16_e32 v196, v114
	v_cvt_f32_f16_sdwa v197, v114 dst_sel:DWORD dst_unused:UNUSED_PAD src0_sel:WORD_1
	v_cvt_f32_f16_e32 v198, v115
	v_cvt_f32_f16_sdwa v199, v115 dst_sel:DWORD dst_unused:UNUSED_PAD src0_sel:WORD_1
	v_cvt_f32_f16_e32 v200, v116
	v_cvt_f32_f16_sdwa v201, v116 dst_sel:DWORD dst_unused:UNUSED_PAD src0_sel:WORD_1
	v_cvt_f32_f16_e32 v202, v117
	v_cvt_f32_f16_sdwa v203, v117 dst_sel:DWORD dst_unused:UNUSED_PAD src0_sel:WORD_1
	v_pk_mul_f32 v[182:183], v[68:69], v[182:183]
	v_pk_mul_f32 v[184:185], v[70:71], v[184:185]
	v_pk_mul_f32 v[186:187], v[64:65], v[186:187]
	v_pk_mul_f32 v[188:189], v[66:67], v[188:189]
	v_pk_add_f32 v[182:183], v[182:183], v[196:197]
	v_pk_add_f32 v[184:185], v[184:185], v[198:199]
	v_pk_add_f32 v[186:187], v[186:187], v[200:201]
	v_pk_add_f32 v[188:189], v[188:189], v[202:203]
	v_cvt_pk_f16_f32 v68, v182, v183
	v_cvt_pk_f16_f32 v69, v184, v185
	v_cvt_pk_f16_f32 v70, v186, v187
	v_cvt_pk_f16_f32 v71, v188, v189
	global_store_dwordx4 v[236:237], v[68:71], off offset:256
	s_waitcnt vmcnt(16)
; __device__ __forceinline__ unsigned cvt_pk_f16(float lo, float hi) { f32x2 v = {lo, hi}; h16x2 b = __builtin_convertvector(v, h16x2); return __builtin_bit_cast(unsigned, b); }
;     __device__ __forceinline__ void operator()(const f32x4 (&acc)[2][2][4][2], const Unit& u, int wr, int wc, int fr, int fq) const {
;     ...
; #pragma unroll
;             for (int ai = 0; ai < 2; ++ai)
; #pragma unroll
;                 for (int mp = 0; mp < 2; ++mp) {
;                     h16x8 gv[2][2], pv[2][2];
; #pragma unroll
;                     for (int mm = 0; mm < 2; ++mm)
; #pragma unroll
;                         for (int bj = 0; bj < 2; ++bj) { const size_t row = (size_t)(row0 + ai * HALF + (2 * mp + mm) * 16);
;                             gv[mm][bj] = *(const h16x8*)(Gn + row * ldg + bj * HALF);
;                             if (n > 0) pv[mm][bj] = *(const h16x8*)(Mg + row * 1024 + col0 + bj * HALF); }
; #pragma unroll
;                     for (int mm = 0; mm < 2; ++mm)
; #pragma unroll
;                         for (int bj = 0; bj < 2; ++bj) { const int m = 2 * mp + mm; const size_t row = (size_t)(row0 + ai * HALF + m * 16);
;                             float o[8];
; #pragma unroll
;                             for (int e = 0; e < 8; ++e) { const float a = e < 4 ? acc[ai][bj][m][0][e] : acc[ai][bj][m][1][e - 4]; o[e] = a * (float)gv[mm][bj][e]; }
;                             if (n > 0) {
; #pragma unroll
;                                 for (int e = 0; e < 8; ++e) o[e] += (float)pv[mm][bj][e]; }
;                             u32x4 w; w.x = cvt_pk_f16(o[0], o[1]); w.y = cvt_pk_f16(o[2], o[3]); w.z = cvt_pk_f16(o[4], o[5]); w.w = cvt_pk_f16(o[6], o[7]);
;                             *(u32x4*)(Mg + row * 1024 + col0 + bj * HALF) = w; }
	v_add_u32_e32 v238, 128, v176
	v_lshlrev_b32_e32 v240, 11, v238
	v_lshl_add_u64 v[236:237], v[180:181], 0, v[240:241]
	v_cvt_f32_f16_e32 v182, v146
	v_cvt_f32_f16_sdwa v183, v146 dst_sel:DWORD dst_unused:UNUSED_PAD src0_sel:WORD_1
	v_cvt_f32_f16_e32 v184, v147
	v_cvt_f32_f16_sdwa v185, v147 dst_sel:DWORD dst_unused:UNUSED_PAD src0_sel:WORD_1
	v_cvt_f32_f16_e32 v186, v148
	v_cvt_f32_f16_sdwa v187, v148 dst_sel:DWORD dst_unused:UNUSED_PAD src0_sel:WORD_1
	v_cvt_f32_f16_e32 v188, v149
	v_cvt_f32_f16_sdwa v189, v149 dst_sel:DWORD dst_unused:UNUSED_PAD src0_sel:WORD_1
	v_cvt_f32_f16_e32 v196, v154
	v_cvt_f32_f16_sdwa v197, v154 dst_sel:DWORD dst_unused:UNUSED_PAD src0_sel:WORD_1
	v_cvt_f32_f16_e32 v198, v155
	v_cvt_f32_f16_sdwa v199, v155 dst_sel:DWORD dst_unused:UNUSED_PAD src0_sel:WORD_1
	v_cvt_f32_f16_e32 v200, v156
	v_cvt_f32_f16_sdwa v201, v156 dst_sel:DWORD dst_unused:UNUSED_PAD src0_sel:WORD_1
	v_cvt_f32_f16_e32 v202, v157
	v_cvt_f32_f16_sdwa v203, v157 dst_sel:DWORD dst_unused:UNUSED_PAD src0_sel:WORD_1
	v_pk_mul_f32 v[182:183], v[60:61], v[182:183]
	v_pk_mul_f32 v[184:185], v[62:63], v[184:185]
	v_pk_mul_f32 v[186:187], v[56:57], v[186:187]
	v_pk_mul_f32 v[188:189], v[58:59], v[188:189]
	v_pk_add_f32 v[182:183], v[182:183], v[196:197]
	v_pk_add_f32 v[184:185], v[184:185], v[198:199]
	v_pk_add_f32 v[186:187], v[186:187], v[200:201]
	v_pk_add_f32 v[188:189], v[188:189], v[202:203]
	v_cvt_pk_f16_f32 v60, v182, v183
	v_cvt_pk_f16_f32 v61, v184, v185
	v_cvt_pk_f16_f32 v62, v186, v187
	v_cvt_pk_f16_f32 v63, v188, v189
	global_store_dwordx4 v[236:237], v[60:63], off
	v_cvt_f32_f16_e32 v182, v150
	v_cvt_f32_f16_sdwa v183, v150 dst_sel:DWORD dst_unused:UNUSED_PAD src0_sel:WORD_1
	v_cvt_f32_f16_e32 v184, v151
	v_cvt_f32_f16_sdwa v185, v151 dst_sel:DWORD dst_unused:UNUSED_PAD src0_sel:WORD_1
	v_cvt_f32_f16_e32 v186, v152
	v_cvt_f32_f16_sdwa v187, v152 dst_sel:DWORD dst_unused:UNUSED_PAD src0_sel:WORD_1
	v_cvt_f32_f16_e32 v188, v153
	v_cvt_f32_f16_sdwa v189, v153 dst_sel:DWORD dst_unused:UNUSED_PAD src0_sel:WORD_1
	v_cvt_f32_f16_e32 v196, v158
	v_cvt_f32_f16_sdwa v197, v158 dst_sel:DWORD dst_unused:UNUSED_PAD src0_sel:WORD_1
	v_cvt_f32_f16_e32 v198, v159
	v_cvt_f32_f16_sdwa v199, v159 dst_sel:DWORD dst_unused:UNUSED_PAD src0_sel:WORD_1
	v_cvt_f32_f16_e32 v200, v160
	v_cvt_f32_f16_sdwa v201, v160 dst_sel:DWORD dst_unused:UNUSED_PAD src0_sel:WORD_1
	v_cvt_f32_f16_e32 v202, v161
	v_cvt_f32_f16_sdwa v203, v161 dst_sel:DWORD dst_unused:UNUSED_PAD src0_sel:WORD_1
	v_pk_mul_f32 v[182:183], v[52:53], v[182:183]
	v_pk_mul_f32 v[184:185], v[54:55], v[184:185]
	v_pk_mul_f32 v[186:187], v[48:49], v[186:187]
	v_pk_mul_f32 v[188:189], v[50:51], v[188:189]
	v_pk_add_f32 v[182:183], v[182:183], v[196:197]
	v_pk_add_f32 v[184:185], v[184:185], v[198:199]
	v_pk_add_f32 v[186:187], v[186:187], v[200:201]
	v_pk_add_f32 v[188:189], v[188:189], v[202:203]
	v_cvt_pk_f16_f32 v52, v182, v183
	v_cvt_pk_f16_f32 v53, v184, v185
	v_cvt_pk_f16_f32 v54, v186, v187
	v_cvt_pk_f16_f32 v55, v188, v189
	global_store_dwordx4 v[236:237], v[52:55], off offset:256
	s_waitcnt vmcnt(14)
	v_add_u32_e32 v238, 144, v176
	v_lshlrev_b32_e32 v240, 11, v238
	v_lshl_add_u64 v[236:237], v[180:181], 0, v[240:241]
	v_cvt_f32_f16_e32 v182, v110
	v_cvt_f32_f16_sdwa v183, v110 dst_sel:DWORD dst_unused:UNUSED_PAD src0_sel:WORD_1
	v_cvt_f32_f16_e32 v184, v111
	v_cvt_f32_f16_sdwa v185, v111 dst_sel:DWORD dst_unused:UNUSED_PAD src0_sel:WORD_1
	v_cvt_f32_f16_e32 v186, v112
	v_cvt_f32_f16_sdwa v187, v112 dst_sel:DWORD dst_unused:UNUSED_PAD src0_sel:WORD_1
	v_cvt_f32_f16_e32 v188, v113
	v_cvt_f32_f16_sdwa v189, v113 dst_sel:DWORD dst_unused:UNUSED_PAD src0_sel:WORD_1
	v_cvt_f32_f16_e32 v196, v102
	v_cvt_f32_f16_sdwa v197, v102 dst_sel:DWORD dst_unused:UNUSED_PAD src0_sel:WORD_1
	v_cvt_f32_f16_e32 v198, v103
	v_cvt_f32_f16_sdwa v199, v103 dst_sel:DWORD dst_unused:UNUSED_PAD src0_sel:WORD_1
	v_cvt_f32_f16_e32 v200, v104
	v_cvt_f32_f16_sdwa v201, v104 dst_sel:DWORD dst_unused:UNUSED_PAD src0_sel:WORD_1
	v_cvt_f32_f16_e32 v202, v105
	v_cvt_f32_f16_sdwa v203, v105 dst_sel:DWORD dst_unused:UNUSED_PAD src0_sel:WORD_1
	v_pk_mul_f32 v[182:183], v[44:45], v[182:183]
	v_pk_mul_f32 v[184:185], v[46:47], v[184:185]
	v_pk_mul_f32 v[186:187], v[40:41], v[186:187]
	v_pk_mul_f32 v[188:189], v[42:43], v[188:189]
	v_pk_add_f32 v[182:183], v[182:183], v[196:197]
	v_pk_add_f32 v[184:185], v[184:185], v[198:199]
	v_pk_add_f32 v[186:187], v[186:187], v[200:201]
	v_pk_add_f32 v[188:189], v[188:189], v[202:203]
	v_cvt_pk_f16_f32 v44, v182, v183
	v_cvt_pk_f16_f32 v45, v184, v185
	v_cvt_pk_f16_f32 v46, v186, v187
	v_cvt_pk_f16_f32 v47, v188, v189
	global_store_dwordx4 v[236:237], v[44:47], off
	v_cvt_f32_f16_e32 v182, v106
	v_cvt_f32_f16_sdwa v183, v106 dst_sel:DWORD dst_unused:UNUSED_PAD src0_sel:WORD_1
	v_cvt_f32_f16_e32 v184, v107
	v_cvt_f32_f16_sdwa v185, v107 dst_sel:DWORD dst_unused:UNUSED_PAD src0_sel:WORD_1
	v_cvt_f32_f16_e32 v186, v108
	v_cvt_f32_f16_sdwa v187, v108 dst_sel:DWORD dst_unused:UNUSED_PAD src0_sel:WORD_1
	v_cvt_f32_f16_e32 v188, v109
	v_cvt_f32_f16_sdwa v189, v109 dst_sel:DWORD dst_unused:UNUSED_PAD src0_sel:WORD_1
	v_cvt_f32_f16_e32 v196, v98
	v_cvt_f32_f16_sdwa v197, v98 dst_sel:DWORD dst_unused:UNUSED_PAD src0_sel:WORD_1
	v_cvt_f32_f16_e32 v198, v99
	v_cvt_f32_f16_sdwa v199, v99 dst_sel:DWORD dst_unused:UNUSED_PAD src0_sel:WORD_1
	v_cvt_f32_f16_e32 v200, v100
	v_cvt_f32_f16_sdwa v201, v100 dst_sel:DWORD dst_unused:UNUSED_PAD src0_sel:WORD_1
	v_cvt_f32_f16_e32 v202, v101
	v_cvt_f32_f16_sdwa v203, v101 dst_sel:DWORD dst_unused:UNUSED_PAD src0_sel:WORD_1
	v_pk_mul_f32 v[182:183], v[28:29], v[182:183]
	v_pk_mul_f32 v[184:185], v[30:31], v[184:185]
	v_pk_mul_f32 v[186:187], v[24:25], v[186:187]
	v_pk_mul_f32 v[188:189], v[26:27], v[188:189]
	v_pk_add_f32 v[182:183], v[182:183], v[196:197]
	v_pk_add_f32 v[184:185], v[184:185], v[198:199]
	v_pk_add_f32 v[186:187], v[186:187], v[200:201]
	v_pk_add_f32 v[188:189], v[188:189], v[202:203]
	v_cvt_pk_f16_f32 v28, v182, v183
	v_cvt_pk_f16_f32 v29, v184, v185
	v_cvt_pk_f16_f32 v30, v186, v187
	v_cvt_pk_f16_f32 v31, v188, v189
	global_store_dwordx4 v[236:237], v[28:31], off offset:256
	s_waitcnt vmcnt(10)
; __device__ __forceinline__ unsigned cvt_pk_f16(float lo, float hi) { f32x2 v = {lo, hi}; h16x2 b = __builtin_convertvector(v, h16x2); return __builtin_bit_cast(unsigned, b); }
;     __device__ __forceinline__ void operator()(const f32x4 (&acc)[2][2][4][2], const Unit& u, int wr, int wc, int fr, int fq) const {
;     ...
; #pragma unroll
;             for (int ai = 0; ai < 2; ++ai)
; #pragma unroll
;                 for (int mp = 0; mp < 2; ++mp) {
;                     h16x8 gv[2][2], pv[2][2];
; #pragma unroll
;                     for (int mm = 0; mm < 2; ++mm)
; #pragma unroll
;                         for (int bj = 0; bj < 2; ++bj) { const size_t row = (size_t)(row0 + ai * HALF + (2 * mp + mm) * 16);
;                             gv[mm][bj] = *(const h16x8*)(Gn + row * ldg + bj * HALF);
;                             if (n > 0) pv[mm][bj] = *(const h16x8*)(Mg + row * 1024 + col0 + bj * HALF); }
; #pragma unroll
;                     for (int mm = 0; mm < 2; ++mm)
; #pragma unroll
;                         for (int bj = 0; bj < 2; ++bj) { const int m = 2 * mp + mm; const size_t row = (size_t)(row0 + ai * HALF + m * 16);
;                             float o[8];
; #pragma unroll
;                             for (int e = 0; e < 8; ++e) { const float a = e < 4 ? acc[ai][bj][m][0][e] : acc[ai][bj][m][1][e - 4]; o[e] = a * (float)gv[mm][bj][e]; }
;                             if (n > 0) {
; #pragma unroll
;                                 for (int e = 0; e < 8; ++e) o[e] += (float)pv[mm][bj][e]; }
;                             u32x4 w; w.x = cvt_pk_f16(o[0], o[1]); w.y = cvt_pk_f16(o[2], o[3]); w.z = cvt_pk_f16(o[4], o[5]); w.w = cvt_pk_f16(o[6], o[7]);
;                             *(u32x4*)(Mg + row * 1024 + col0 + bj * HALF) = w; }
	v_add_u32_e32 v238, 160, v176
	v_lshlrev_b32_e32 v240, 11, v238
	v_lshl_add_u64 v[236:237], v[180:181], 0, v[240:241]
	v_cvt_f32_f16_e32 v182, v130
	v_cvt_f32_f16_sdwa v183, v130 dst_sel:DWORD dst_unused:UNUSED_PAD src0_sel:WORD_1
	v_cvt_f32_f16_e32 v184, v131
	v_cvt_f32_f16_sdwa v185, v131 dst_sel:DWORD dst_unused:UNUSED_PAD src0_sel:WORD_1
	v_cvt_f32_f16_e32 v186, v132
	v_cvt_f32_f16_sdwa v187, v132 dst_sel:DWORD dst_unused:UNUSED_PAD src0_sel:WORD_1
	v_cvt_f32_f16_e32 v188, v133
	v_cvt_f32_f16_sdwa v189, v133 dst_sel:DWORD dst_unused:UNUSED_PAD src0_sel:WORD_1
	v_cvt_f32_f16_e32 v196, v138
	v_cvt_f32_f16_sdwa v197, v138 dst_sel:DWORD dst_unused:UNUSED_PAD src0_sel:WORD_1
	v_cvt_f32_f16_e32 v198, v139
	v_cvt_f32_f16_sdwa v199, v139 dst_sel:DWORD dst_unused:UNUSED_PAD src0_sel:WORD_1
	v_cvt_f32_f16_e32 v200, v140
	v_cvt_f32_f16_sdwa v201, v140 dst_sel:DWORD dst_unused:UNUSED_PAD src0_sel:WORD_1
	v_cvt_f32_f16_e32 v202, v141
	v_cvt_f32_f16_sdwa v203, v141 dst_sel:DWORD dst_unused:UNUSED_PAD src0_sel:WORD_1
	v_pk_mul_f32 v[182:183], v[20:21], v[182:183]
	v_pk_mul_f32 v[184:185], v[22:23], v[184:185]
	v_pk_mul_f32 v[186:187], v[16:17], v[186:187]
	v_pk_mul_f32 v[188:189], v[18:19], v[188:189]
	v_pk_add_f32 v[182:183], v[182:183], v[196:197]
	v_pk_add_f32 v[184:185], v[184:185], v[198:199]
	v_pk_add_f32 v[186:187], v[186:187], v[200:201]
	v_pk_add_f32 v[188:189], v[188:189], v[202:203]
	v_cvt_pk_f16_f32 v20, v182, v183
	v_cvt_pk_f16_f32 v21, v184, v185
	v_cvt_pk_f16_f32 v22, v186, v187
	v_cvt_pk_f16_f32 v23, v188, v189
	global_store_dwordx4 v[236:237], v[20:23], off
	v_cvt_f32_f16_e32 v182, v134
	v_cvt_f32_f16_sdwa v183, v134 dst_sel:DWORD dst_unused:UNUSED_PAD src0_sel:WORD_1
	v_cvt_f32_f16_e32 v184, v135
	v_cvt_f32_f16_sdwa v185, v135 dst_sel:DWORD dst_unused:UNUSED_PAD src0_sel:WORD_1
	v_cvt_f32_f16_e32 v186, v136
	v_cvt_f32_f16_sdwa v187, v136 dst_sel:DWORD dst_unused:UNUSED_PAD src0_sel:WORD_1
	v_cvt_f32_f16_e32 v188, v137
	v_cvt_f32_f16_sdwa v189, v137 dst_sel:DWORD dst_unused:UNUSED_PAD src0_sel:WORD_1
	v_cvt_f32_f16_e32 v196, v142
	v_cvt_f32_f16_sdwa v197, v142 dst_sel:DWORD dst_unused:UNUSED_PAD src0_sel:WORD_1
	v_cvt_f32_f16_e32 v198, v143
	v_cvt_f32_f16_sdwa v199, v143 dst_sel:DWORD dst_unused:UNUSED_PAD src0_sel:WORD_1
	v_cvt_f32_f16_e32 v200, v144
	v_cvt_f32_f16_sdwa v201, v144 dst_sel:DWORD dst_unused:UNUSED_PAD src0_sel:WORD_1
	v_cvt_f32_f16_e32 v202, v145
	v_cvt_f32_f16_sdwa v203, v145 dst_sel:DWORD dst_unused:UNUSED_PAD src0_sel:WORD_1
	v_pk_mul_f32 v[182:183], v[32:33], v[182:183]
	v_pk_mul_f32 v[184:185], v[34:35], v[184:185]
	v_pk_mul_f32 v[186:187], v[36:37], v[186:187]
	v_pk_mul_f32 v[188:189], v[38:39], v[188:189]
	v_pk_add_f32 v[182:183], v[182:183], v[196:197]
	v_pk_add_f32 v[184:185], v[184:185], v[198:199]
	v_pk_add_f32 v[186:187], v[186:187], v[200:201]
	v_pk_add_f32 v[188:189], v[188:189], v[202:203]
	v_cvt_pk_f16_f32 v32, v182, v183
	v_cvt_pk_f16_f32 v33, v184, v185
	v_cvt_pk_f16_f32 v34, v186, v187
	v_cvt_pk_f16_f32 v35, v188, v189
	global_store_dwordx4 v[236:237], v[32:35], off offset:256
	s_waitcnt vmcnt(8)
	v_add_u32_e32 v238, 176, v176
	v_lshlrev_b32_e32 v240, 11, v238
	v_lshl_add_u64 v[236:237], v[180:181], 0, v[240:241]
	v_cvt_f32_f16_e32 v182, v92
	v_cvt_f32_f16_sdwa v183, v92 dst_sel:DWORD dst_unused:UNUSED_PAD src0_sel:WORD_1
	v_cvt_f32_f16_e32 v184, v93
	v_cvt_f32_f16_sdwa v185, v93 dst_sel:DWORD dst_unused:UNUSED_PAD src0_sel:WORD_1
	v_cvt_f32_f16_e32 v186, v94
	v_cvt_f32_f16_sdwa v187, v94 dst_sel:DWORD dst_unused:UNUSED_PAD src0_sel:WORD_1
	v_cvt_f32_f16_e32 v188, v95
	v_cvt_f32_f16_sdwa v189, v95 dst_sel:DWORD dst_unused:UNUSED_PAD src0_sel:WORD_1
	v_cvt_f32_f16_e32 v196, v84
	v_cvt_f32_f16_sdwa v197, v84 dst_sel:DWORD dst_unused:UNUSED_PAD src0_sel:WORD_1
	v_cvt_f32_f16_e32 v198, v85
	v_cvt_f32_f16_sdwa v199, v85 dst_sel:DWORD dst_unused:UNUSED_PAD src0_sel:WORD_1
	v_cvt_f32_f16_e32 v200, v86
	v_cvt_f32_f16_sdwa v201, v86 dst_sel:DWORD dst_unused:UNUSED_PAD src0_sel:WORD_1
	v_cvt_f32_f16_e32 v202, v87
	v_cvt_f32_f16_sdwa v203, v87 dst_sel:DWORD dst_unused:UNUSED_PAD src0_sel:WORD_1
	v_pk_mul_f32 v[182:183], v[4:5], v[182:183]
	v_pk_mul_f32 v[184:185], v[6:7], v[184:185]
	v_pk_mul_f32 v[186:187], v[0:1], v[186:187]
	v_pk_mul_f32 v[188:189], v[2:3], v[188:189]
	v_pk_add_f32 v[182:183], v[182:183], v[196:197]
	v_pk_add_f32 v[184:185], v[184:185], v[198:199]
	v_pk_add_f32 v[186:187], v[186:187], v[200:201]
	v_pk_add_f32 v[188:189], v[188:189], v[202:203]
	v_cvt_pk_f16_f32 v4, v182, v183
	v_cvt_pk_f16_f32 v5, v184, v185
	v_cvt_pk_f16_f32 v6, v186, v187
	v_cvt_pk_f16_f32 v7, v188, v189
	global_store_dwordx4 v[236:237], v[4:7], off
	v_cvt_f32_f16_e32 v182, v88
	v_cvt_f32_f16_sdwa v183, v88 dst_sel:DWORD dst_unused:UNUSED_PAD src0_sel:WORD_1
	v_cvt_f32_f16_e32 v184, v89
	v_cvt_f32_f16_sdwa v185, v89 dst_sel:DWORD dst_unused:UNUSED_PAD src0_sel:WORD_1
	v_cvt_f32_f16_e32 v186, v90
	v_cvt_f32_f16_sdwa v187, v90 dst_sel:DWORD dst_unused:UNUSED_PAD src0_sel:WORD_1
	v_cvt_f32_f16_e32 v188, v91
	v_cvt_f32_f16_sdwa v189, v91 dst_sel:DWORD dst_unused:UNUSED_PAD src0_sel:WORD_1
	v_cvt_f32_f16_e32 v196, v80
	v_cvt_f32_f16_sdwa v197, v80 dst_sel:DWORD dst_unused:UNUSED_PAD src0_sel:WORD_1
	v_cvt_f32_f16_e32 v198, v81
	v_cvt_f32_f16_sdwa v199, v81 dst_sel:DWORD dst_unused:UNUSED_PAD src0_sel:WORD_1
	v_cvt_f32_f16_e32 v200, v82
	v_cvt_f32_f16_sdwa v201, v82 dst_sel:DWORD dst_unused:UNUSED_PAD src0_sel:WORD_1
	v_cvt_f32_f16_e32 v202, v83
	v_cvt_f32_f16_sdwa v203, v83 dst_sel:DWORD dst_unused:UNUSED_PAD src0_sel:WORD_1
	v_pk_mul_f32 v[182:183], v[8:9], v[182:183]
	v_pk_mul_f32 v[184:185], v[10:11], v[184:185]
	v_pk_mul_f32 v[186:187], v[12:13], v[186:187]
	v_pk_mul_f32 v[188:189], v[14:15], v[188:189]
	v_pk_add_f32 v[182:183], v[182:183], v[196:197]
	v_pk_add_f32 v[184:185], v[184:185], v[198:199]
	v_pk_add_f32 v[186:187], v[186:187], v[200:201]
	v_pk_add_f32 v[188:189], v[188:189], v[202:203]
	v_cvt_pk_f16_f32 v8, v182, v183
	v_cvt_pk_f16_f32 v9, v184, v185
	v_cvt_pk_f16_f32 v10, v186, v187
	v_cvt_pk_f16_f32 v11, v188, v189
	global_store_dwordx4 v[236:237], v[8:11], off offset:256
	s_branch .Lbrepi_done
; __device__ __forceinline__ unsigned cvt_pk_f16(float lo, float hi) { f32x2 v = {lo, hi}; h16x2 b = __builtin_convertvector(v, h16x2); return __builtin_bit_cast(unsigned, b); }
;     __device__ __forceinline__ void operator()(const f32x4 (&acc)[2][2][4][2], const Unit& u, int wr, int wc, int fr, int fq) const {
;     ...
; #pragma unroll
;             for (int ai = 0; ai < 2; ++ai)
; #pragma unroll
;                 for (int mp = 0; mp < 2; ++mp) {
;                     h16x8 gv[2][2], pv[2][2];
; #pragma unroll
;                     for (int mm = 0; mm < 2; ++mm)
; #pragma unroll
;                         for (int bj = 0; bj < 2; ++bj) { const size_t row = (size_t)(row0 + ai * HALF + (2 * mp + mm) * 16);
;                             gv[mm][bj] = *(const h16x8*)(Gn + row * ldg + bj * HALF);
;                             if (n > 0) pv[mm][bj] = *(const h16x8*)(Mg + row * 1024 + col0 + bj * HALF); }
; #pragma unroll
;                     for (int mm = 0; mm < 2; ++mm)
; #pragma unroll
;                         for (int bj = 0; bj < 2; ++bj) { const int m = 2 * mp + mm; const size_t row = (size_t)(row0 + ai * HALF + m * 16);
;                             float o[8];
; #pragma unroll
;                             for (int e = 0; e < 8; ++e) { const float a = e < 4 ? acc[ai][bj][m][0][e] : acc[ai][bj][m][1][e - 4]; o[e] = a * (float)gv[mm][bj][e]; }
;                             if (n > 0) {
; #pragma unroll
;                                 for (int e = 0; e < 8; ++e) o[e] += (float)pv[mm][bj][e]; }
;                             u32x4 w; w.x = cvt_pk_f16(o[0], o[1]); w.y = cvt_pk_f16(o[2], o[3]); w.z = cvt_pk_f16(o[4], o[5]); w.w = cvt_pk_f16(o[6], o[7]);
;                             *(u32x4*)(Mg + row * 1024 + col0 + bj * HALF) = w; }
.Lbrepi_n0:
	v_readlane_b32 s40, v254, 46
	v_readlane_b32 s41, v254, 47
	v_mov_b32_e32 v241, 0
	s_nop 1
	v_lshl_add_u64 v[180:181], v[178:179], 1, s[40:41]
	v_mov_b32_e32 v238, v176
	v_mad_i64_i32 v[234:235], s[0:1], v238, s91, v[174:175]
	global_load_dwordx4 v[130:133], v[234:235], off
	global_load_dwordx4 v[134:137], v[234:235], off offset:256
	v_add_u32_e32 v238, 16, v176
	v_mad_i64_i32 v[234:235], s[0:1], v238, s91, v[174:175]
	global_load_dwordx4 v[146:149], v[234:235], off
	global_load_dwordx4 v[150:153], v[234:235], off offset:256
	s_waitcnt vmcnt(2)
	v_mov_b32_e32 v238, v176
	v_lshlrev_b32_e32 v240, 11, v238
	v_lshl_add_u64 v[236:237], v[180:181], 0, v[240:241]
	v_cvt_f32_f16_e32 v182, v130
	v_cvt_f32_f16_sdwa v183, v130 dst_sel:DWORD dst_unused:UNUSED_PAD src0_sel:WORD_1
	v_cvt_f32_f16_e32 v184, v131
	v_cvt_f32_f16_sdwa v185, v131 dst_sel:DWORD dst_unused:UNUSED_PAD src0_sel:WORD_1
	v_cvt_f32_f16_e32 v186, v132
	v_cvt_f32_f16_sdwa v187, v132 dst_sel:DWORD dst_unused:UNUSED_PAD src0_sel:WORD_1
	v_cvt_f32_f16_e32 v188, v133
	v_cvt_f32_f16_sdwa v189, v133 dst_sel:DWORD dst_unused:UNUSED_PAD src0_sel:WORD_1
	v_pk_mul_f32 v[182:183], v[126:127], v[182:183]
	v_pk_mul_f32 v[184:185], v[128:129], v[184:185]
	v_pk_mul_f32 v[186:187], v[122:123], v[186:187]
	v_pk_mul_f32 v[188:189], v[124:125], v[188:189]
	v_cvt_pk_f16_f32 v126, v182, v183
	v_cvt_pk_f16_f32 v127, v184, v185
	v_cvt_pk_f16_f32 v128, v186, v187
	v_cvt_pk_f16_f32 v129, v188, v189
	global_store_dwordx4 v[236:237], v[126:129], off
	v_cvt_f32_f16_e32 v182, v134
	v_cvt_f32_f16_sdwa v183, v134 dst_sel:DWORD dst_unused:UNUSED_PAD src0_sel:WORD_1
	v_cvt_f32_f16_e32 v184, v135
	v_cvt_f32_f16_sdwa v185, v135 dst_sel:DWORD dst_unused:UNUSED_PAD src0_sel:WORD_1
	v_cvt_f32_f16_e32 v186, v136
	v_cvt_f32_f16_sdwa v187, v136 dst_sel:DWORD dst_unused:UNUSED_PAD src0_sel:WORD_1
	v_cvt_f32_f16_e32 v188, v137
	v_cvt_f32_f16_sdwa v189, v137 dst_sel:DWORD dst_unused:UNUSED_PAD src0_sel:WORD_1
	v_pk_mul_f32 v[182:183], v[118:119], v[182:183]
	v_pk_mul_f32 v[184:185], v[120:121], v[184:185]
	v_pk_mul_f32 v[186:187], v[114:115], v[186:187]
	v_pk_mul_f32 v[188:189], v[116:117], v[188:189]
	v_cvt_pk_f16_f32 v118, v182, v183
	v_cvt_pk_f16_f32 v119, v184, v185
	v_cvt_pk_f16_f32 v120, v186, v187
	v_cvt_pk_f16_f32 v121, v188, v189
	global_store_dwordx4 v[236:237], v[118:121], off offset:256
	v_add_u32_e32 v238, 32, v176
	v_mad_i64_i32 v[234:235], s[0:1], v238, s91, v[174:175]
	global_load_dwordx4 v[130:133], v[234:235], off
	global_load_dwordx4 v[134:137], v[234:235], off offset:256
	s_nop 1
	v_add_u32_e32 v238, 48, v176
	v_mad_i64_i32 v[234:235], s[0:1], v238, s91, v[174:175]
	global_load_dwordx4 v[126:129], v[234:235], off
	global_load_dwordx4 v[122:125], v[234:235], off offset:256
	s_waitcnt vmcnt(6)
	v_add_u32_e32 v238, 16, v176
	v_lshlrev_b32_e32 v240, 11, v238
	v_lshl_add_u64 v[236:237], v[180:181], 0, v[240:241]
	v_cvt_f32_f16_e32 v182, v146
	v_cvt_f32_f16_sdwa v183, v146 dst_sel:DWORD dst_unused:UNUSED_PAD src0_sel:WORD_1
	v_cvt_f32_f16_e32 v184, v147
	v_cvt_f32_f16_sdwa v185, v147 dst_sel:DWORD dst_unused:UNUSED_PAD src0_sel:WORD_1
	v_cvt_f32_f16_e32 v186, v148
	v_cvt_f32_f16_sdwa v187, v148 dst_sel:DWORD dst_unused:UNUSED_PAD src0_sel:WORD_1
	v_cvt_f32_f16_e32 v188, v149
	v_cvt_f32_f16_sdwa v189, v149 dst_sel:DWORD dst_unused:UNUSED_PAD src0_sel:WORD_1
	v_pk_mul_f32 v[182:183], v[110:111], v[182:183]
	v_pk_mul_f32 v[184:185], v[112:113], v[184:185]
	v_pk_mul_f32 v[186:187], v[106:107], v[186:187]
	v_pk_mul_f32 v[188:189], v[108:109], v[188:189]
	v_cvt_pk_f16_f32 v110, v182, v183
	v_cvt_pk_f16_f32 v111, v184, v185
	v_cvt_pk_f16_f32 v112, v186, v187
	v_cvt_pk_f16_f32 v113, v188, v189
	global_store_dwordx4 v[236:237], v[110:113], off
	v_cvt_f32_f16_e32 v182, v150
	v_cvt_f32_f16_sdwa v183, v150 dst_sel:DWORD dst_unused:UNUSED_PAD src0_sel:WORD_1
	v_cvt_f32_f16_e32 v184, v151
	v_cvt_f32_f16_sdwa v185, v151 dst_sel:DWORD dst_unused:UNUSED_PAD src0_sel:WORD_1
	v_cvt_f32_f16_e32 v186, v152
	v_cvt_f32_f16_sdwa v187, v152 dst_sel:DWORD dst_unused:UNUSED_PAD src0_sel:WORD_1
	v_cvt_f32_f16_e32 v188, v153
	v_cvt_f32_f16_sdwa v189, v153 dst_sel:DWORD dst_unused:UNUSED_PAD src0_sel:WORD_1
	v_pk_mul_f32 v[182:183], v[102:103], v[182:183]
	v_pk_mul_f32 v[184:185], v[104:105], v[184:185]
	v_pk_mul_f32 v[186:187], v[98:99], v[186:187]
	v_pk_mul_f32 v[188:189], v[100:101], v[188:189]
	v_cvt_pk_f16_f32 v102, v182, v183
	v_cvt_pk_f16_f32 v103, v184, v185
	v_cvt_pk_f16_f32 v104, v186, v187
	v_cvt_pk_f16_f32 v105, v188, v189
	global_store_dwordx4 v[236:237], v[102:105], off offset:256
	v_add_u32_e32 v238, 128, v176
	v_mad_i64_i32 v[234:235], s[0:1], v238, s91, v[174:175]
	global_load_dwordx4 v[146:149], v[234:235], off
	global_load_dwordx4 v[150:153], v[234:235], off offset:256
	s_nop 1
	v_add_u32_e32 v238, 144, v176
	v_mad_i64_i32 v[234:235], s[0:1], v238, s91, v[174:175]
	global_load_dwordx4 v[110:113], v[234:235], off
	global_load_dwordx4 v[106:109], v[234:235], off offset:256
	s_waitcnt vmcnt(8)
; __device__ __forceinline__ unsigned cvt_pk_f16(float lo, float hi) { f32x2 v = {lo, hi}; h16x2 b = __builtin_convertvector(v, h16x2); return __builtin_bit_cast(unsigned, b); }
;     __device__ __forceinline__ void operator()(const f32x4 (&acc)[2][2][4][2], const Unit& u, int wr, int wc, int fr, int fq) const {
;     ...
; #pragma unroll
;             for (int ai = 0; ai < 2; ++ai)
; #pragma unroll
;                 for (int mp = 0; mp < 2; ++mp) {
;                     h16x8 gv[2][2], pv[2][2];
; #pragma unroll
;                     for (int mm = 0; mm < 2; ++mm)
; #pragma unroll
;                         for (int bj = 0; bj < 2; ++bj) { const size_t row = (size_t)(row0 + ai * HALF + (2 * mp + mm) * 16);
;                             gv[mm][bj] = *(const h16x8*)(Gn + row * ldg + bj * HALF);
;                             if (n > 0) pv[mm][bj] = *(const h16x8*)(Mg + row * 1024 + col0 + bj * HALF); }
; #pragma unroll
;                     for (int mm = 0; mm < 2; ++mm)
; #pragma unroll
;                         for (int bj = 0; bj < 2; ++bj) { const int m = 2 * mp + mm; const size_t row = (size_t)(row0 + ai * HALF + m * 16);
;                             float o[8];
; #pragma unroll
;                             for (int e = 0; e < 8; ++e) { const float a = e < 4 ? acc[ai][bj][m][0][e] : acc[ai][bj][m][1][e - 4]; o[e] = a * (float)gv[mm][bj][e]; }
;                             if (n > 0) {
; #pragma unroll
;                                 for (int e = 0; e < 8; ++e) o[e] += (float)pv[mm][bj][e]; }
;                             u32x4 w; w.x = cvt_pk_f16(o[0], o[1]); w.y = cvt_pk_f16(o[2], o[3]); w.z = cvt_pk_f16(o[4], o[5]); w.w = cvt_pk_f16(o[6], o[7]);
;                             *(u32x4*)(Mg + row * 1024 + col0 + bj * HALF) = w; }
	v_add_u32_e32 v238, 32, v176
	v_lshlrev_b32_e32 v240, 11, v238
	v_lshl_add_u64 v[236:237], v[180:181], 0, v[240:241]
	v_cvt_f32_f16_e32 v182, v130
	v_cvt_f32_f16_sdwa v183, v130 dst_sel:DWORD dst_unused:UNUSED_PAD src0_sel:WORD_1
	v_cvt_f32_f16_e32 v184, v131
	v_cvt_f32_f16_sdwa v185, v131 dst_sel:DWORD dst_unused:UNUSED_PAD src0_sel:WORD_1
	v_cvt_f32_f16_e32 v186, v132
	v_cvt_f32_f16_sdwa v187, v132 dst_sel:DWORD dst_unused:UNUSED_PAD src0_sel:WORD_1
	v_cvt_f32_f16_e32 v188, v133
	v_cvt_f32_f16_sdwa v189, v133 dst_sel:DWORD dst_unused:UNUSED_PAD src0_sel:WORD_1
	v_pk_mul_f32 v[182:183], v[92:93], v[182:183]
	v_pk_mul_f32 v[184:185], v[94:95], v[184:185]
	v_pk_mul_f32 v[186:187], v[88:89], v[186:187]
	v_pk_mul_f32 v[188:189], v[90:91], v[188:189]
	v_cvt_pk_f16_f32 v92, v182, v183
	v_cvt_pk_f16_f32 v93, v184, v185
	v_cvt_pk_f16_f32 v94, v186, v187
	v_cvt_pk_f16_f32 v95, v188, v189
	global_store_dwordx4 v[236:237], v[92:95], off
	v_cvt_f32_f16_e32 v182, v134
	v_cvt_f32_f16_sdwa v183, v134 dst_sel:DWORD dst_unused:UNUSED_PAD src0_sel:WORD_1
	v_cvt_f32_f16_e32 v184, v135
	v_cvt_f32_f16_sdwa v185, v135 dst_sel:DWORD dst_unused:UNUSED_PAD src0_sel:WORD_1
	v_cvt_f32_f16_e32 v186, v136
	v_cvt_f32_f16_sdwa v187, v136 dst_sel:DWORD dst_unused:UNUSED_PAD src0_sel:WORD_1
	v_cvt_f32_f16_e32 v188, v137
	v_cvt_f32_f16_sdwa v189, v137 dst_sel:DWORD dst_unused:UNUSED_PAD src0_sel:WORD_1
	v_pk_mul_f32 v[182:183], v[84:85], v[182:183]
	v_pk_mul_f32 v[184:185], v[86:87], v[184:185]
	v_pk_mul_f32 v[186:187], v[80:81], v[186:187]
	v_pk_mul_f32 v[188:189], v[82:83], v[188:189]
	v_cvt_pk_f16_f32 v84, v182, v183
	v_cvt_pk_f16_f32 v85, v184, v185
	v_cvt_pk_f16_f32 v86, v186, v187
	v_cvt_pk_f16_f32 v87, v188, v189
	global_store_dwordx4 v[236:237], v[84:87], off offset:256
	v_add_u32_e32 v238, 160, v176
	v_mad_i64_i32 v[234:235], s[0:1], v238, s91, v[174:175]
	global_load_dwordx4 v[130:133], v[234:235], off
	global_load_dwordx4 v[134:137], v[234:235], off offset:256
	s_nop 1
	v_add_u32_e32 v238, 176, v176
	v_mad_i64_i32 v[234:235], s[0:1], v238, s91, v[174:175]
	global_load_dwordx4 v[92:95], v[234:235], off
	global_load_dwordx4 v[88:91], v[234:235], off offset:256
	s_waitcnt vmcnt(12)
	v_add_u32_e32 v238, 48, v176
	v_lshlrev_b32_e32 v240, 11, v238
	v_lshl_add_u64 v[236:237], v[180:181], 0, v[240:241]
	v_cvt_f32_f16_e32 v182, v126
	v_cvt_f32_f16_sdwa v183, v126 dst_sel:DWORD dst_unused:UNUSED_PAD src0_sel:WORD_1
	v_cvt_f32_f16_e32 v184, v127
	v_cvt_f32_f16_sdwa v185, v127 dst_sel:DWORD dst_unused:UNUSED_PAD src0_sel:WORD_1
	v_cvt_f32_f16_e32 v186, v128
	v_cvt_f32_f16_sdwa v187, v128 dst_sel:DWORD dst_unused:UNUSED_PAD src0_sel:WORD_1
	v_cvt_f32_f16_e32 v188, v129
	v_cvt_f32_f16_sdwa v189, v129 dst_sel:DWORD dst_unused:UNUSED_PAD src0_sel:WORD_1
	v_pk_mul_f32 v[182:183], v[76:77], v[182:183]
	v_pk_mul_f32 v[184:185], v[78:79], v[184:185]
	v_pk_mul_f32 v[186:187], v[72:73], v[186:187]
	v_pk_mul_f32 v[188:189], v[74:75], v[188:189]
	v_cvt_pk_f16_f32 v76, v182, v183
	v_cvt_pk_f16_f32 v77, v184, v185
	v_cvt_pk_f16_f32 v78, v186, v187
	v_cvt_pk_f16_f32 v79, v188, v189
	global_store_dwordx4 v[236:237], v[76:79], off
	v_cvt_f32_f16_e32 v182, v122
	v_cvt_f32_f16_sdwa v183, v122 dst_sel:DWORD dst_unused:UNUSED_PAD src0_sel:WORD_1
	v_cvt_f32_f16_e32 v184, v123
	v_cvt_f32_f16_sdwa v185, v123 dst_sel:DWORD dst_unused:UNUSED_PAD src0_sel:WORD_1
	v_cvt_f32_f16_e32 v186, v124
	v_cvt_f32_f16_sdwa v187, v124 dst_sel:DWORD dst_unused:UNUSED_PAD src0_sel:WORD_1
	v_cvt_f32_f16_e32 v188, v125
	v_cvt_f32_f16_sdwa v189, v125 dst_sel:DWORD dst_unused:UNUSED_PAD src0_sel:WORD_1
	v_pk_mul_f32 v[182:183], v[68:69], v[182:183]
	v_pk_mul_f32 v[184:185], v[70:71], v[184:185]
	v_pk_mul_f32 v[186:187], v[64:65], v[186:187]
	v_pk_mul_f32 v[188:189], v[66:67], v[188:189]
	v_cvt_pk_f16_f32 v68, v182, v183
	v_cvt_pk_f16_f32 v69, v184, v185
	v_cvt_pk_f16_f32 v70, v186, v187
	v_cvt_pk_f16_f32 v71, v188, v189
	global_store_dwordx4 v[236:237], v[68:71], off offset:256
	s_waitcnt vmcnt(10)
	v_add_u32_e32 v238, 128, v176
	v_lshlrev_b32_e32 v240, 11, v238
	v_lshl_add_u64 v[236:237], v[180:181], 0, v[240:241]
	v_cvt_f32_f16_e32 v182, v146
	v_cvt_f32_f16_sdwa v183, v146 dst_sel:DWORD dst_unused:UNUSED_PAD src0_sel:WORD_1
	v_cvt_f32_f16_e32 v184, v147
	v_cvt_f32_f16_sdwa v185, v147 dst_sel:DWORD dst_unused:UNUSED_PAD src0_sel:WORD_1
	v_cvt_f32_f16_e32 v186, v148
	v_cvt_f32_f16_sdwa v187, v148 dst_sel:DWORD dst_unused:UNUSED_PAD src0_sel:WORD_1
	v_cvt_f32_f16_e32 v188, v149
	v_cvt_f32_f16_sdwa v189, v149 dst_sel:DWORD dst_unused:UNUSED_PAD src0_sel:WORD_1
	v_pk_mul_f32 v[182:183], v[60:61], v[182:183]
	v_pk_mul_f32 v[184:185], v[62:63], v[184:185]
	v_pk_mul_f32 v[186:187], v[56:57], v[186:187]
	v_pk_mul_f32 v[188:189], v[58:59], v[188:189]
	v_cvt_pk_f16_f32 v60, v182, v183
	v_cvt_pk_f16_f32 v61, v184, v185
	v_cvt_pk_f16_f32 v62, v186, v187
	v_cvt_pk_f16_f32 v63, v188, v189
	global_store_dwordx4 v[236:237], v[60:63], off
	v_cvt_f32_f16_e32 v182, v150
	v_cvt_f32_f16_sdwa v183, v150 dst_sel:DWORD dst_unused:UNUSED_PAD src0_sel:WORD_1
	v_cvt_f32_f16_e32 v184, v151
	v_cvt_f32_f16_sdwa v185, v151 dst_sel:DWORD dst_unused:UNUSED_PAD src0_sel:WORD_1
	v_cvt_f32_f16_e32 v186, v152
	v_cvt_f32_f16_sdwa v187, v152 dst_sel:DWORD dst_unused:UNUSED_PAD src0_sel:WORD_1
	v_cvt_f32_f16_e32 v188, v153
	v_cvt_f32_f16_sdwa v189, v153 dst_sel:DWORD dst_unused:UNUSED_PAD src0_sel:WORD_1
	v_pk_mul_f32 v[182:183], v[52:53], v[182:183]
	v_pk_mul_f32 v[184:185], v[54:55], v[184:185]
	v_pk_mul_f32 v[186:187], v[48:49], v[186:187]
	v_pk_mul_f32 v[188:189], v[50:51], v[188:189]
	v_cvt_pk_f16_f32 v52, v182, v183
	v_cvt_pk_f16_f32 v53, v184, v185
	v_cvt_pk_f16_f32 v54, v186, v187
	v_cvt_pk_f16_f32 v55, v188, v189
	global_store_dwordx4 v[236:237], v[52:55], off offset:256
	s_waitcnt vmcnt(10)
; __device__ __forceinline__ unsigned cvt_pk_f16(float lo, float hi) { f32x2 v = {lo, hi}; h16x2 b = __builtin_convertvector(v, h16x2); return __builtin_bit_cast(unsigned, b); }
;     __device__ __forceinline__ void operator()(const f32x4 (&acc)[2][2][4][2], const Unit& u, int wr, int wc, int fr, int fq) const {
;     ...
; #pragma unroll
;             for (int ai = 0; ai < 2; ++ai)
; #pragma unroll
;                 for (int mp = 0; mp < 2; ++mp) {
;                     h16x8 gv[2][2], pv[2][2];
; #pragma unroll
;                     for (int mm = 0; mm < 2; ++mm)
; #pragma unroll
;                         for (int bj = 0; bj < 2; ++bj) { const size_t row = (size_t)(row0 + ai * HALF + (2 * mp + mm) * 16);
;                             gv[mm][bj] = *(const h16x8*)(Gn + row * ldg + bj * HALF);
;                             if (n > 0) pv[mm][bj] = *(const h16x8*)(Mg + row * 1024 + col0 + bj * HALF); }
; #pragma unroll
;                     for (int mm = 0; mm < 2; ++mm)
; #pragma unroll
;                         for (int bj = 0; bj < 2; ++bj) { const int m = 2 * mp + mm; const size_t row = (size_t)(row0 + ai * HALF + m * 16);
;                             float o[8];
; #pragma unroll
;                             for (int e = 0; e < 8; ++e) { const float a = e < 4 ? acc[ai][bj][m][0][e] : acc[ai][bj][m][1][e - 4]; o[e] = a * (float)gv[mm][bj][e]; }
;                             if (n > 0) {
; #pragma unroll
;                                 for (int e = 0; e < 8; ++e) o[e] += (float)pv[mm][bj][e]; }
;                             u32x4 w; w.x = cvt_pk_f16(o[0], o[1]); w.y = cvt_pk_f16(o[2], o[3]); w.z = cvt_pk_f16(o[4], o[5]); w.w = cvt_pk_f16(o[6], o[7]);
;                             *(u32x4*)(Mg + row * 1024 + col0 + bj * HALF) = w; }
	v_add_u32_e32 v238, 144, v176
	v_lshlrev_b32_e32 v240, 11, v238
	v_lshl_add_u64 v[236:237], v[180:181], 0, v[240:241]
	v_cvt_f32_f16_e32 v182, v110
	v_cvt_f32_f16_sdwa v183, v110 dst_sel:DWORD dst_unused:UNUSED_PAD src0_sel:WORD_1
	v_cvt_f32_f16_e32 v184, v111
	v_cvt_f32_f16_sdwa v185, v111 dst_sel:DWORD dst_unused:UNUSED_PAD src0_sel:WORD_1
	v_cvt_f32_f16_e32 v186, v112
	v_cvt_f32_f16_sdwa v187, v112 dst_sel:DWORD dst_unused:UNUSED_PAD src0_sel:WORD_1
	v_cvt_f32_f16_e32 v188, v113
	v_cvt_f32_f16_sdwa v189, v113 dst_sel:DWORD dst_unused:UNUSED_PAD src0_sel:WORD_1
	v_pk_mul_f32 v[182:183], v[44:45], v[182:183]
	v_pk_mul_f32 v[184:185], v[46:47], v[184:185]
	v_pk_mul_f32 v[186:187], v[40:41], v[186:187]
	v_pk_mul_f32 v[188:189], v[42:43], v[188:189]
	v_cvt_pk_f16_f32 v44, v182, v183
	v_cvt_pk_f16_f32 v45, v184, v185
	v_cvt_pk_f16_f32 v46, v186, v187
	v_cvt_pk_f16_f32 v47, v188, v189
	global_store_dwordx4 v[236:237], v[44:47], off
	v_cvt_f32_f16_e32 v182, v106
	v_cvt_f32_f16_sdwa v183, v106 dst_sel:DWORD dst_unused:UNUSED_PAD src0_sel:WORD_1
	v_cvt_f32_f16_e32 v184, v107
	v_cvt_f32_f16_sdwa v185, v107 dst_sel:DWORD dst_unused:UNUSED_PAD src0_sel:WORD_1
	v_cvt_f32_f16_e32 v186, v108
	v_cvt_f32_f16_sdwa v187, v108 dst_sel:DWORD dst_unused:UNUSED_PAD src0_sel:WORD_1
	v_cvt_f32_f16_e32 v188, v109
	v_cvt_f32_f16_sdwa v189, v109 dst_sel:DWORD dst_unused:UNUSED_PAD src0_sel:WORD_1
	v_pk_mul_f32 v[182:183], v[28:29], v[182:183]
	v_pk_mul_f32 v[184:185], v[30:31], v[184:185]
	v_pk_mul_f32 v[186:187], v[24:25], v[186:187]
	v_pk_mul_f32 v[188:189], v[26:27], v[188:189]
	v_cvt_pk_f16_f32 v28, v182, v183
	v_cvt_pk_f16_f32 v29, v184, v185
	v_cvt_pk_f16_f32 v30, v186, v187
	v_cvt_pk_f16_f32 v31, v188, v189
	global_store_dwordx4 v[236:237], v[28:31], off offset:256
	s_waitcnt vmcnt(8)
	v_add_u32_e32 v238, 160, v176
	v_lshlrev_b32_e32 v240, 11, v238
	v_lshl_add_u64 v[236:237], v[180:181], 0, v[240:241]
	v_cvt_f32_f16_e32 v182, v130
	v_cvt_f32_f16_sdwa v183, v130 dst_sel:DWORD dst_unused:UNUSED_PAD src0_sel:WORD_1
	v_cvt_f32_f16_e32 v184, v131
	v_cvt_f32_f16_sdwa v185, v131 dst_sel:DWORD dst_unused:UNUSED_PAD src0_sel:WORD_1
	v_cvt_f32_f16_e32 v186, v132
	v_cvt_f32_f16_sdwa v187, v132 dst_sel:DWORD dst_unused:UNUSED_PAD src0_sel:WORD_1
	v_cvt_f32_f16_e32 v188, v133
	v_cvt_f32_f16_sdwa v189, v133 dst_sel:DWORD dst_unused:UNUSED_PAD src0_sel:WORD_1
	v_pk_mul_f32 v[182:183], v[20:21], v[182:183]
	v_pk_mul_f32 v[184:185], v[22:23], v[184:185]
	v_pk_mul_f32 v[186:187], v[16:17], v[186:187]
	v_pk_mul_f32 v[188:189], v[18:19], v[188:189]
	v_cvt_pk_f16_f32 v20, v182, v183
	v_cvt_pk_f16_f32 v21, v184, v185
	v_cvt_pk_f16_f32 v22, v186, v187
	v_cvt_pk_f16_f32 v23, v188, v189
	global_store_dwordx4 v[236:237], v[20:23], off
	v_cvt_f32_f16_e32 v182, v134
	v_cvt_f32_f16_sdwa v183, v134 dst_sel:DWORD dst_unused:UNUSED_PAD src0_sel:WORD_1
	v_cvt_f32_f16_e32 v184, v135
	v_cvt_f32_f16_sdwa v185, v135 dst_sel:DWORD dst_unused:UNUSED_PAD src0_sel:WORD_1
	v_cvt_f32_f16_e32 v186, v136
	v_cvt_f32_f16_sdwa v187, v136 dst_sel:DWORD dst_unused:UNUSED_PAD src0_sel:WORD_1
	v_cvt_f32_f16_e32 v188, v137
	v_cvt_f32_f16_sdwa v189, v137 dst_sel:DWORD dst_unused:UNUSED_PAD src0_sel:WORD_1
	v_pk_mul_f32 v[182:183], v[32:33], v[182:183]
	v_pk_mul_f32 v[184:185], v[34:35], v[184:185]
	v_pk_mul_f32 v[186:187], v[36:37], v[186:187]
	v_pk_mul_f32 v[188:189], v[38:39], v[188:189]
	v_cvt_pk_f16_f32 v32, v182, v183
	v_cvt_pk_f16_f32 v33, v184, v185
	v_cvt_pk_f16_f32 v34, v186, v187
	v_cvt_pk_f16_f32 v35, v188, v189
	global_store_dwordx4 v[236:237], v[32:35], off offset:256
	s_waitcnt vmcnt(8)
	v_add_u32_e32 v238, 176, v176
	v_lshlrev_b32_e32 v240, 11, v238
	v_lshl_add_u64 v[236:237], v[180:181], 0, v[240:241]
	v_cvt_f32_f16_e32 v182, v92
	v_cvt_f32_f16_sdwa v183, v92 dst_sel:DWORD dst_unused:UNUSED_PAD src0_sel:WORD_1
	v_cvt_f32_f16_e32 v184, v93
	v_cvt_f32_f16_sdwa v185, v93 dst_sel:DWORD dst_unused:UNUSED_PAD src0_sel:WORD_1
	v_cvt_f32_f16_e32 v186, v94
	v_cvt_f32_f16_sdwa v187, v94 dst_sel:DWORD dst_unused:UNUSED_PAD src0_sel:WORD_1
	v_cvt_f32_f16_e32 v188, v95
	v_cvt_f32_f16_sdwa v189, v95 dst_sel:DWORD dst_unused:UNUSED_PAD src0_sel:WORD_1
	v_pk_mul_f32 v[182:183], v[4:5], v[182:183]
	v_pk_mul_f32 v[184:185], v[6:7], v[184:185]
	v_pk_mul_f32 v[186:187], v[0:1], v[186:187]
	v_pk_mul_f32 v[188:189], v[2:3], v[188:189]
	v_cvt_pk_f16_f32 v4, v182, v183
	v_cvt_pk_f16_f32 v5, v184, v185
	v_cvt_pk_f16_f32 v6, v186, v187
	v_cvt_pk_f16_f32 v7, v188, v189
	global_store_dwordx4 v[236:237], v[4:7], off
	v_cvt_f32_f16_e32 v182, v88
	v_cvt_f32_f16_sdwa v183, v88 dst_sel:DWORD dst_unused:UNUSED_PAD src0_sel:WORD_1
	v_cvt_f32_f16_e32 v184, v89
	v_cvt_f32_f16_sdwa v185, v89 dst_sel:DWORD dst_unused:UNUSED_PAD src0_sel:WORD_1
	v_cvt_f32_f16_e32 v186, v90
	v_cvt_f32_f16_sdwa v187, v90 dst_sel:DWORD dst_unused:UNUSED_PAD src0_sel:WORD_1
	v_cvt_f32_f16_e32 v188, v91
	v_cvt_f32_f16_sdwa v189, v91 dst_sel:DWORD dst_unused:UNUSED_PAD src0_sel:WORD_1
	v_pk_mul_f32 v[182:183], v[8:9], v[182:183]
	v_pk_mul_f32 v[184:185], v[10:11], v[184:185]
	v_pk_mul_f32 v[186:187], v[12:13], v[186:187]
	v_pk_mul_f32 v[188:189], v[14:15], v[188:189]
	v_cvt_pk_f16_f32 v8, v182, v183
	v_cvt_pk_f16_f32 v9, v184, v185
	v_cvt_pk_f16_f32 v10, v186, v187
	v_cvt_pk_f16_f32 v11, v188, v189
	global_store_dwordx4 v[236:237], v[8:11], off offset:256
	s_branch .Lbrepi_done
